# speedup vs baseline: 1.0033x; 1.0033x over previous
.LBB2_3:
	s_lshl_b32 s63, s53, 1
	s_add_i32 s61, s63, 2
	s_sub_i32 s2, s61, s40
	s_lshl_b32 s60, s53, 7
	s_min_i32 s62, s33, s2
	s_cmp_eq_u32 s55, 0
	s_cselect_b32 s79, 0, s62
	s_cmp_lt_i32 s2, 1
	s_waitcnt vmcnt(0)
	s_barrier
	s_cbranch_scc1 .LBB2_21
	s_add_i32 s63, s63, s55
	v_lshl_or_b32 v11, s63, 6, v83
	v_add_u32_e32 v10, s60, v82
	v_or_b32_e32 v12, 2, v11
	v_cmp_gt_i32_e64 s[6:7], v12, v10
	v_or_b32_e32 v12, 3, v11
	v_cmp_gt_i32_e64 s[8:9], v12, v10
	v_or_b32_e32 v12, 16, v11
	v_cmp_gt_i32_e64 s[10:11], v12, v10
	v_or_b32_e32 v12, 17, v11
	v_cmp_gt_i32_e64 s[12:13], v12, v10
	v_or_b32_e32 v12, 18, v11
	v_cmp_gt_i32_e64 s[14:15], v12, v10
	v_or_b32_e32 v12, 19, v11
	v_cmp_gt_i32_e64 s[16:17], v12, v10
	v_or_b32_e32 v12, 32, v11
	v_cmp_gt_i32_e64 s[18:19], v12, v10
	v_or_b32_e32 v12, 33, v11
	v_cmp_gt_i32_e64 s[20:21], v12, v10
	v_or_b32_e32 v12, 34, v11
	v_cmp_gt_i32_e64 s[22:23], v12, v10
	v_or_b32_e32 v12, 35, v11
	v_cmp_gt_i32_e64 s[24:25], v12, v10
	v_or_b32_e32 v12, 48, v11
	s_sub_i32 s37, s56, s40
	v_cmp_gt_i32_e64 s[26:27], v12, v10
	v_or_b32_e32 v12, 49, v11
	s_min_i32 s37, s33, s37
	v_cmp_gt_i32_e64 s[2:3], v11, v10
	v_cmp_lt_i32_e64 s[4:5], v11, v10
	v_cmp_gt_i32_e64 s[28:29], v12, v10
	v_or_b32_e32 v12, 50, v11
	v_or_b32_e32 v11, 51, v11
	s_max_i32 s37, s37, 1
	s_lshl_b64 s[38:39], s[40:41], 13
	v_mov_b32_e32 v67, 0
	v_cmp_gt_i32_e64 s[30:31], v12, v10
	v_cmp_gt_i32_e64 s[34:35], v11, v10
	s_mov_b32 s64, 1
	s_sub_i32 s65, 0, s37
	s_add_i32 s66, s40, s57
	s_add_u32 s68, s70, s38
	s_addc_u32 s69, s71, s39
	s_add_u32 s74, s72, s38
	s_addc_u32 s75, s73, s39
	v_mov_b32_e32 v14, v51
	v_mov_b32_e32 v15, v51
	v_mov_b32_e32 v16, v51
	v_mov_b32_e32 v17, v51
	s_mov_b64 s[38:39], -1
	v_mov_b32_e32 v30, 0
	v_mov_b32_e32 v31, v67
	v_mov_b32_e32 v32, v67
	v_mov_b32_e32 v33, v67
	v_mov_b32_e32 v26, 0
	v_mov_b32_e32 v27, v67
	v_mov_b32_e32 v28, v67
	v_mov_b32_e32 v29, v67
	v_mov_b32_e32 v22, v67
	v_mov_b32_e32 v23, v67
	v_mov_b32_e32 v24, v67
	v_mov_b32_e32 v25, v67
	v_mov_b32_e32 v18, v67
	v_mov_b32_e32 v19, v67
	v_mov_b32_e32 v20, v67
	v_mov_b32_e32 v21, v67
	v_mov_b32_e32 v10, v67
	v_mov_b32_e32 v11, v67
	v_mov_b32_e32 v12, v67
	v_mov_b32_e32 v13, v67
	s_mov_b32 s37, 0
	s_mov_b32 s48, s40
	v_mov_b32_e32 v114, v57
	v_mov_b32_e32 v115, v81
	s_cmp_gt_u32 s48, s63
	s_branch .Lattn_after_rdv

.LBB2_6:
	s_add_i32 s64, s64, 1
	s_add_u32 s68, s68, 0x2000
	s_addc_u32 s69, s69, 0
	s_add_u32 s74, s74, 0x2000
	s_addc_u32 s75, s75, 0
	s_add_i32 s37, s65, s64
	s_cmp_eq_u32 s37, 1
	s_cbranch_scc1 .Lattn_last_step
.LBB2_7:
	s_add_i32 s37, s64, -1
	s_and_b32 s37, s37, 1
	s_lshl_b32 s37, s37, 14
	s_add_i32 s48, s40, s64
	s_add_i32 s48, s48, -1
	v_or_b32_e32 v114, s37, v57
	v_or_b32_e32 v115, s37, v81
	s_cmp_gt_u32 s48, s63
	s_waitcnt vmcnt(0) lgkmcnt(0)
	s_barrier
.Lattn_after_rdv:
	s_cbranch_scc1 .Lattn_skip_tile
	ds_read_b128 v[34:37], v114
	ds_read_b128 v[38:41], v114 offset:2048
	ds_read_b128 v[42:45], v114 offset:4096
	ds_read_b128 v[110:113], v115 offset:2048
	ds_read_b128 v[46:49], v114 offset:6144
	s_cmp_lt_i32 s64, s79
	s_cbranch_scc1 .Lattn_do_dma

.LBB2_12:
	v_max3_f32 v69, v46, v47, v48
	s_and_b64 vcc, exec, s[38:39]
	s_nop 1
	v_max3_f32 v71, v49, v42, v43
	v_max3_f32 v69, v69, v44, v45
	v_max3_f32 v71, v71, v38, v39
	v_max3_f32 v69, v69, v40, v41
	v_max3_f32 v71, v71, v34, v35
	v_max3_f32 v69, v69, v36, v37
	v_max_f32_e32 v69, v69, v71
	s_cbranch_vccnz .Lattn_first_tile
	v_cmp_lt_f32_e32 vcc, s58, v69
	s_nop 1
	s_cbranch_vccz .LBB2_5
	v_mov_b32_e32 v71, v69
	s_nop 1
	v_permlane16_swap_b32_e32 v69, v71
	v_max_f32_e32 v69, v69, v71
	v_mov_b32_e32 v71, v69
	s_nop 1
	v_permlane32_swap_b32_e32 v69, v71
	v_max_f32_e32 v69, v69, v71
	v_max_f32_e32 v71, v69, v69
	v_max_f32_e32 v80, 0, v71
	s_branch .Lattn_rescale

.Lattn_do_dma:
	s_xor_b32 s48, s37, 0x4000
	s_add_i32 s48, s78, s48
	s_mov_b32 m0, s48
	s_nop 0
	global_load_lds_dwordx4 v64, s[68:69]
	s_add_i32 m0, s48, 0x400
	s_nop 0
	global_load_lds_dwordx4 v65, s[68:69]
	s_add_i32 m0, s48, 0x2000
	s_nop 0
	global_load_lds_dwordx4 v64, s[74:75]
	s_add_i32 m0, s48, 0x2400
	s_nop 0
	global_load_lds_dwordx4 v65, s[74:75]
	s_branch .Lattn_no_dma
.Lattn_last_step:
	s_waitcnt vmcnt(0) lgkmcnt(0)
	s_barrier
